# MLA: stage-barrier vmcnt wait counted so the side job's own loads/store stay in flight across the barrier (on top of spread schedule + permanent ones rows)
# speedup vs baseline: 1.0169x; 1.0042x over previous
; DEV void sj_tick(const Params& p, int layer, SideJob& sj, LAS char* lds, int tid) {
;     ...
;     if (ph == 0) {
;         const int krow = tid >> 4, c4 = (tid & 15) * 4;
;         const float* a0 = (d.mode == 0 || d.mode == 2) ? d.s0 + (size_t)(d.k0 + krow) * d.ld + d.nt * 64 + c4
;                                         : ((c4 < 32) ? d.s0 + (size_t)(d.k0 + krow) * 512 + d.nt * 32 + c4 : d.s1 + (size_t)(d.k0 + krow) * 512 + d.nt * 32 + c4 - 32);
;         sj.v0 = *(const f32x4*)a0; sj.v1 = *(const f32x4*)(a0 + (size_t)32 * d.ld);
.LBB0_810:
	s_lshl_b32 s30, s20, 7
	v_lshl_add_u64 v[98:99], v[100:101], 0, s[30:31]
	global_load_dwordx4 v[182:185], v[100:101], off
	global_load_dwordx4 v[186:189], v[98:99], off
	s_mov_b32 s100, 2
	s_mov_b32 s21, s36
	s_mov_b32 s57, s33

; #define LAS __attribute__((address_space(3)))
; #define WAITV(n) asm volatile("s_waitcnt vmcnt(%0)" ::"n"(n) : "memory")
; #define SBAR() do { asm volatile("s_waitcnt lgkmcnt(0)" ::: "memory"); __builtin_amdgcn_s_barrier(); asm volatile("" ::: "memory"); } while (0)
; DEV float ex2(float x) { return __builtin_amdgcn_exp2f(x); }
; template <int VAR> DEV void mla_step(f32x16& C0, f32x16& C1, f32x16& P0, f32x16& P1, f32x16& o0, f32x16& o1, f32x16& lacc,
;                   const v8i (&qf)[2], const f32x16& cini, LAS char* kp, LAS char* vp, v8i& pw) {
;     v8i kf[2], vf[2];
;     const v8i ones8 = {0x38383838, 0x38383838, 0x38383838, 0x38383838, 0x38383838, 0x38383838, 0x38383838, 0x38383838};
;     kf[0] = mla_kf8(kp, 0, 0); kf[1] = mla_kf8(kp, 1, 0);
;     MLA_SB();
; #pragma unroll
;     for (int g = 0; g < 4; ++g) {
;         const int kb = g & 1, sx = g >> 1;
;         if (kb) C1 = MFMA8(kf[1], qf[sx], sx == 0 ? cini : C1); else C0 = MFMA8(kf[0], qf[sx], sx == 0 ? cini : C0);
;         if (g < 2) kf[kb] = mla_kf8(kp, kb, 1);
;         if (g >= 2) vf[g - 2] = mla_vf8(vp, g - 2);
; #pragma unroll
;         for (int j = 0; j < 2; ++j) { const int w = 2 * g + j, e = 4 * w;
;             if (VAR == 3) pw[w] = __builtin_bit_cast(int, (e < 16) ? P0[e] : P1[e - 16]);
;             else pw[w] = (int)((e < 16) ? pk_bf8x4(P0[e], P0[e + 1], P0[e + 2], P0[e + 3], pw[w]) : pk_bf8x4(P1[e - 16], P1[e - 15], P1[e - 14], P1[e - 13], pw[w])); }
;         if (g == 3) MLA_PIN(pw);
;         MLA_SB();
;     }
; #pragma unroll
;     for (int g = 0; g < 3; ++g) {
;         if (g == 0) o0 = MFMA8PV(vf[0], pw, o0); else if (g == 1) o1 = MFMA8PV(vf[1], pw, o1); else lacc = MFMA8PV(ones8, pw, lacc);
;         const int e0 = (g * 32) / 3, e1 = ((g + 1) * 32) / 3;
; #pragma unroll
;         for (int e = e0; e < e1; ++e) { if (VAR == 2 || VAR == 3) continue; if (e < 16) C0[e] = ex2(C0[e]); else C1[e - 16] = ex2(C1[e - 16]); }
;         if (g < 2) MLA_PIN(C0);
;         if (g > 0) MLA_PIN(C1);
;         MLA_SB();
;     }
; }
; template <int VAR> DEV void mla_unit(const Params& p, int layer, int b, int hd, int tokbase, int t0, int t1, LAS char* lds, SideJob& sj) {
;     ...
;         if (s + 1 < ns) {
;             const int nslot = (slot == 2) ? 0 : slot + 1;
;             WAITV(0); SBAR();
;             if (s + 2 < ns) MLA_ISSUE(t0 + s + 2, (nslot == 2) ? 0 : nslot + 1);
.LBB0_812:
	s_mul_i32 s2, s62, 0x6000
	v_add_u32_e32 v172, s2, v200
	ds_read_b128 v[98:101], v172 offset:8192
	ds_read_b128 v[106:109], v172 offset:8704
	ds_read_b128 v[102:105], v172 offset:9216
	ds_read_b128 v[110:113], v172 offset:9728
	v_cvt_pk_bf8_f32 v146, v82, v83
	v_cvt_pk_bf8_f32 v147, v86, v87
	v_exp_f32_e32 v69, v69
	v_exp_f32_e32 v70, v70
	v_exp_f32_e32 v71, v71
	s_waitcnt lgkmcnt(1)
	v_mfma_scale_f32_32x32x64_f8f6f4 v[114:129], v[98:105], v[138:145], v[2:17], v209, v208 op_sel_hi:[0,0,0]
	ds_read_b128 v[154:157], v172 offset:12288
	ds_read_b128 v[158:161], v172 offset:13312
	v_cvt_pk_bf8_f32 v146, v84, v85 op_sel:[0,0,1]
	v_cvt_pk_bf8_f32 v147, v88, v89 op_sel:[0,0,1]
	v_cvt_pk_bf8_f32 v148, v90, v91
	v_cvt_pk_bf8_f32 v149, v94, v95
	ds_read_b128 v[82:85], v172 offset:12800
	ds_read_b128 v[86:89], v172 offset:13824
	v_exp_f32_e32 v72, v72
	v_exp_f32_e32 v73, v73
	s_waitcnt lgkmcnt(4)
	v_mfma_scale_f32_32x32x64_f8f6f4 v[98:113], v[106:113], v[138:145], v[2:17], v209, v208 op_sel_hi:[0,0,0]
	v_cvt_pk_bf8_f32 v148, v92, v93 op_sel:[0,0,1]
	v_cvt_pk_bf8_f32 v149, v96, v97 op_sel:[0,0,1]
	ds_read_b128 v[90:93], v172 offset:16384
	ds_read_b128 v[94:97], v172 offset:17408
	v_exp_f32_e32 v74, v74
	v_exp_f32_e32 v75, v75
	v_exp_f32_e32 v76, v76
	s_waitcnt lgkmcnt(4)
	v_mfma_scale_f32_32x32x64_f8f6f4 v[114:129], v[154:161], v[130:137], v[114:129], v209, v208 op_sel_hi:[0,0,0]
	v_exp_f32_e32 v77, v77
	v_exp_f32_e32 v78, v78
	v_exp_f32_e32 v79, v79
	v_exp_f32_e32 v80, v80
	v_exp_f32_e32 v81, v81
	s_waitcnt lgkmcnt(2)
	v_mfma_scale_f32_32x32x64_f8f6f4 v[98:113], v[82:89], v[130:137], v[98:113], v209, v208 op_sel_hi:[0,0,0]
	v_cvt_pk_bf8_f32 v150, v66, v67
	v_cvt_pk_bf8_f32 v151, v70, v71
	v_cvt_pk_bf8_f32 v150, v68, v69 op_sel:[0,0,1]
	v_cvt_pk_bf8_f32 v151, v72, v73 op_sel:[0,0,1]
	v_cvt_pk_bf8_f32 v152, v74, v75
	v_cvt_pk_bf8_f32 v153, v78, v79
	v_cvt_pk_bf8_f32 v152, v76, v77 op_sel:[0,0,1]
	v_cvt_pk_bf8_f32 v153, v80, v81 op_sel:[0,0,1]
	ds_read_b128 v[66:69], v172 offset:16896
	ds_read_b128 v[70:73], v172 offset:17920
	s_waitcnt lgkmcnt(2)
	v_mfma_scale_f32_32x32x64_f8f6f4 v[50:65], v[90:97], v[146:153], v[50:65], v209, v209 op_sel_hi:[0,0,0] blgp:1
	s_nop 0
	v_exp_f32_e32 v114, v114
	v_exp_f32_e32 v115, v115
	v_exp_f32_e32 v116, v116
	v_exp_f32_e32 v117, v117
	v_exp_f32_e32 v118, v118
	v_exp_f32_e32 v119, v119
	s_waitcnt lgkmcnt(0)
	v_mfma_scale_f32_32x32x64_f8f6f4 v[18:33], v[66:73], v[146:153], v[18:33], v209, v209 op_sel_hi:[0,0,0] blgp:1
	v_exp_f32_e32 v120, v120
	v_exp_f32_e32 v121, v121
	v_exp_f32_e32 v122, v122
	v_exp_f32_e32 v123, v123
	v_exp_f32_e32 v124, v124
	v_exp_f32_e32 v125, v125
	v_mfma_scale_f32_32x32x64_f8f6f4 v[34:49], v[210:217], v[146:153], v[34:49], v209, v209 op_sel_hi:[0,0,0] blgp:1
	v_exp_f32_e32 v126, v126
	v_exp_f32_e32 v127, v127
	v_exp_f32_e32 v128, v128
	v_exp_f32_e32 v129, v129
	v_exp_f32_e32 v98, v98
	v_exp_f32_e32 v99, v99
	v_exp_f32_e32 v100, v100
	s_add_i32 s61, s61, 1
	s_add_i32 s2, s62, 1
	s_cmp_lg_u32 s62, 2
	s_cselect_b32 s62, s2, 0
	s_mul_i32 s64, s62, 0x6000
	s_add_i32 s2, s64, 0x6000
	s_cmp_eq_u32 s62, 2
	s_cselect_b64 s[8:9], -1, 0
	s_cmp_eq_u32 s100, 0
	s_cbranch_scc1 .Lmla_w0
	s_cmp_eq_u32 s100, 1
	s_cbranch_scc1 .Lmla_w1
	s_waitcnt vmcnt(2)
	s_branch .Lmla_wd
.Lmla_w1:
	s_waitcnt vmcnt(1)
	s_branch .Lmla_wd

; #define LAS __attribute__((address_space(3)))
; #define WAITV(n) asm volatile("s_waitcnt vmcnt(%0)" ::"n"(n) : "memory")
; #define SBAR() do { asm volatile("s_waitcnt lgkmcnt(0)" ::: "memory"); __builtin_amdgcn_s_barrier(); asm volatile("" ::: "memory"); } while (0)
; #define MLA_ISSUE(t_, st_) do { const unsigned char* s_ = imgs + (size_t)(t_) * MLA_IMG + wid * (STG / 8) + lane * 16; const unsigned d_ = ldsw + (unsigned)((st_) * STG); \
;     _Pragma("unroll") for (int i_ = 0; i_ < STG / 8192; ++i_) glds16a(s_ + i_ * 1024, d_ + i_ * 1024); } while (0)
; DEV void sj_tick(const Params& p, int layer, SideJob& sj, LAS char* lds, int tid) {
;     LAS float* tile = (LAS float*)(lds + SJ_TILE_OFF);
;     const int ph = sj.g & 3; ++sj.g;
;     if (sj.le >= 64 || ph == 3) return;
;     const SjDesc d = sj_desc(p, layer, sj.le, sj.j);
; template <int VAR> DEV void mla_unit(const Params& p, int layer, int b, int hd, int tokbase, int t0, int t1, LAS char* lds, SideJob& sj) {
;     ...
;     for (int s = 0; s < ns; ++s) {
;         sj_tick(p, layer, sj, lds, tid);
;         { LAS char* base = lds + slot * STG; mla_step<VAR>(sB0, sB1, sA0, sA1, o0, o1, lacc, qf, cini, base + MLA_KSUB + koffl, base + voffl, pw); }
;         if (s + 1 < ns) {
;             const int nslot = (slot == 2) ? 0 : slot + 1;
;             WAITV(0); SBAR();
;             if (s + 2 < ns) MLA_ISSUE(t0 + s + 2, (nslot == 2) ? 0 : nslot + 1);
;             { LAS char* nb = lds + nslot * STG; LAS char* ob = lds + slot * STG; mla_step<VAR>(sA0, sA1, sB0, sB1, o0, o1, lacc, qf, cini, nb + koffl, ob + MLA_VSUB + voffl, pw); }
.Lmla_wd:
	s_and_b64 s[20:21], s[8:9], exec
	s_waitcnt lgkmcnt(0)
	s_barrier
	s_cselect_b32 s2, 0, s2
	s_add_i32 s2, s2, s60
	s_mov_b32 s3, m0
	s_mov_b32 m0, s2
	v_add_u32_e32 v173, s64, v200
	ds_read_b128 v[66:69], v173
	ds_read_b128 v[74:77], v173 offset:512
	ds_read_b128 v[70:73], v173 offset:1024
	ds_read_b128 v[78:81], v173 offset:1536
	v_cvt_pk_bf8_f32 v146, v114, v115
	v_cvt_pk_bf8_f32 v147, v118, v119
	v_exp_f32_e32 v101, v101
	v_exp_f32_e32 v102, v102
	v_exp_f32_e32 v103, v103
	s_waitcnt lgkmcnt(1)
	v_mfma_scale_f32_32x32x64_f8f6f4 v[82:97], v[66:73], v[138:145], v[2:17], v209, v208 op_sel_hi:[0,0,0]
	global_load_lds_dwordx4 v[162:163], off
	ds_read_b128 v[164:167], v173 offset:4096
	ds_read_b128 v[168:171], v173 offset:5120
	v_cvt_pk_bf8_f32 v146, v116, v117 op_sel:[0,0,1]
	v_cvt_pk_bf8_f32 v147, v120, v121 op_sel:[0,0,1]
	v_cvt_pk_bf8_f32 v148, v122, v123
	v_cvt_pk_bf8_f32 v149, v126, v127
	ds_read_b128 v[114:117], v173 offset:4608
	ds_read_b128 v[118:121], v173 offset:5632
	v_exp_f32_e32 v104, v104
	v_exp_f32_e32 v105, v105
	s_waitcnt lgkmcnt(4)
	v_mfma_scale_f32_32x32x64_f8f6f4 v[66:81], v[74:81], v[138:145], v[2:17], v209, v208 op_sel_hi:[0,0,0]
	global_load_lds_dwordx4 v[162:163], off offset:1024
	v_cvt_pk_bf8_f32 v148, v124, v125 op_sel:[0,0,1]
	v_cvt_pk_bf8_f32 v149, v128, v129 op_sel:[0,0,1]
	ds_read_b128 v[122:125], v172 offset:20480
	ds_read_b128 v[126:129], v172 offset:21504
	v_exp_f32_e32 v106, v106
	v_exp_f32_e32 v107, v107
	v_exp_f32_e32 v108, v108
	s_waitcnt lgkmcnt(4)
	v_mfma_scale_f32_32x32x64_f8f6f4 v[82:97], v[164:171], v[130:137], v[82:97], v209, v208 op_sel_hi:[0,0,0]
	global_load_lds_dwordx4 v[162:163], off offset:2048
	s_mov_b32 m0, s3
	v_exp_f32_e32 v109, v109
	v_exp_f32_e32 v110, v110
	v_exp_f32_e32 v111, v111
	v_exp_f32_e32 v112, v112
	v_exp_f32_e32 v113, v113
	s_waitcnt lgkmcnt(2)
	v_mfma_scale_f32_32x32x64_f8f6f4 v[66:81], v[114:121], v[130:137], v[66:81], v209, v208 op_sel_hi:[0,0,0]
	v_cvt_pk_bf8_f32 v150, v98, v99
	v_cvt_pk_bf8_f32 v151, v102, v103
	v_cvt_pk_bf8_f32 v150, v100, v101 op_sel:[0,0,1]
	v_cvt_pk_bf8_f32 v151, v104, v105 op_sel:[0,0,1]
	v_cvt_pk_bf8_f32 v152, v106, v107
	v_cvt_pk_bf8_f32 v153, v110, v111
	v_cvt_pk_bf8_f32 v152, v108, v109 op_sel:[0,0,1]
	v_cvt_pk_bf8_f32 v153, v112, v113 op_sel:[0,0,1]
	ds_read_b128 v[98:101], v172 offset:20992
	ds_read_b128 v[102:105], v172 offset:22016
	s_waitcnt lgkmcnt(2)
	v_mfma_scale_f32_32x32x64_f8f6f4 v[50:65], v[122:129], v[146:153], v[50:65], v209, v209 op_sel_hi:[0,0,0] blgp:1
	s_nop 0
	v_exp_f32_e32 v82, v82
	v_exp_f32_e32 v83, v83
	v_exp_f32_e32 v84, v84
	v_exp_f32_e32 v85, v85
	v_exp_f32_e32 v86, v86
	v_exp_f32_e32 v87, v87
	s_waitcnt lgkmcnt(0)
	v_mfma_scale_f32_32x32x64_f8f6f4 v[18:33], v[98:105], v[146:153], v[18:33], v209, v209 op_sel_hi:[0,0,0] blgp:1
	v_exp_f32_e32 v88, v88
	v_exp_f32_e32 v89, v89
	v_exp_f32_e32 v90, v90
	v_exp_f32_e32 v91, v91
	v_exp_f32_e32 v92, v92
	v_exp_f32_e32 v93, v93
	v_mfma_scale_f32_32x32x64_f8f6f4 v[34:49], v[210:217], v[146:153], v[34:49], v209, v209 op_sel_hi:[0,0,0] blgp:1
	v_exp_f32_e32 v94, v94
	v_exp_f32_e32 v95, v95
	v_exp_f32_e32 v96, v96
	v_exp_f32_e32 v97, v97
	v_exp_f32_e32 v66, v66
	v_exp_f32_e32 v67, v67
	v_exp_f32_e32 v68, v68
	s_mov_b64 s[20:21], 0x6000
	s_cmpk_lg_i32 s61, 0x80
	v_lshl_add_u64 v[162:163], v[162:163], 0, s[20:21]
	s_cbranch_scc0 .LBB0_835
.LBB0_813:
	s_mov_b32 s100, 0
	s_add_i32 s2, s29, s61
	s_and_b32 s63, s2, 3
	s_cmp_gt_i32 s33, 63
	s_cselect_b64 s[8:9], -1, 0
	s_cmp_eq_u32 s63, 3
	s_cselect_b64 s[20:21], -1, 0
	s_or_b64 s[8:9], s[8:9], s[20:21]
	s_and_b64 vcc, exec, s[8:9]
	s_cbranch_vccnz .LBB0_812
	s_add_i32 s20, s33, s12
	s_cmpk_lt_i32 s36, 0x100
	s_cselect_b64 s[50:51], -1, 0
	s_lshl_b32 s58, s36, 6
	s_cmpk_gt_i32 s36, 0xff
	s_mov_b64 s[56:57], -1
	s_cbranch_scc1 .LBB0_816
	s_ashr_i32 s21, s20, 31
	s_lshl_b64 s[52:53], s[20:21], 21
	s_add_u32 s8, s44, s52
	s_addc_u32 s9, s45, s53
	s_add_u32 s52, s46, s52
	s_addc_u32 s53, s47, s53
	s_lshl_b64 s[54:55], s[20:21], 20
	s_add_u32 s54, s13, s54
	s_addc_u32 s55, s16, s55
	s_and_b32 s30, s58, 0x3c0
	s_ashr_i32 s64, s36, 4
	s_mov_b64 s[56:57], 0

; DEV unsigned pk_fp8x4(float a, float b, float c, float d) { int w = __builtin_amdgcn_cvt_pk_fp8_f32(a, b, 0, false); w = __builtin_amdgcn_cvt_pk_fp8_f32(c, d, w, true); return (unsigned)w; }
; DEV void sj_advance(SideJob& sj) { sj.j += (int)gridDim.x; while (sj.j >= 384) { sj.j -= 384; ++sj.le; } }
; DEV void sj_tick(const Params& p, int layer, SideJob& sj, LAS char* lds, int tid) {
;     ...
;     } else {
;         const int nl = tid >> 3, kc = tid & 7, blk = nl >> 5, rho = nl & 31; int cl;
;         if (d.mode == 0) cl = 32 * blk + perm32(rho);
;         else if (d.mode >= 2) cl = nl;
;         else { const int i = (rho & 3) + 4 * (rho >> 3), hh = (rho >> 2) & 1; cl = (i < 8 ? 0 : 32) + 16 * blk + 8 * hh + (i & 7); }
;         float v[8];
; #pragma unroll
;         for (int j = 0; j < 8; ++j) v[j] = tile[(8 * kc + j) * 65 + cl];
;         *(u32x2*)(d.dst + (size_t)(d.nt * 64 + nl) * d.ld_dst + d.k0 + 8 * kc) = (u32x2){pk_fp8x4(v[0] * 32.f, v[1] * 32.f, v[2] * 32.f, v[3] * 32.f), pk_fp8x4(v[4] * 32.f, v[5] * 32.f, v[6] * 32.f, v[7] * 32.f)};
;         sj_advance(sj);
.LBB0_819:
	s_cmp_lg_u32 s63, 1
	s_cbranch_scc0 .LBB0_822
	v_add_u32_e32 v102, v196, v197
	ds_read2_b32 v[98:99], v102 offset1:65
	ds_read2_b32 v[100:101], v102 offset0:130 offset1:195
	v_add_u32_e32 v104, 0x400, v102
	ds_read2_b32 v[102:103], v104 offset0:4 offset1:69
	ds_read2_b32 v[104:105], v104 offset0:134 offset1:199
	s_add_i32 s21, s36, s94
	s_waitcnt lgkmcnt(3)
	v_mul_f32_e32 v106, 0x42000000, v98
	v_mul_f32_e32 v99, 0x42000000, v99
	v_mov_b32_e32 v98, 0
	v_cvt_pk_fp8_f32 v98, v106, v99
	s_waitcnt lgkmcnt(1)
	v_mul_f32_e32 v102, 0x42000000, v102
	v_mul_f32_e32 v103, 0x42000000, v103
	v_mov_b32_e32 v99, 0
	v_cvt_pk_fp8_f32 v99, v102, v103
	v_mul_f32_e32 v100, 0x42000000, v100
	v_mul_f32_e32 v101, 0x42000000, v101
	v_cvt_pk_fp8_f32 v98, v100, v101 op_sel:[0,0,1]
	s_waitcnt lgkmcnt(0)
	v_mul_f32_e32 v100, 0x42000000, v104
	v_mul_f32_e32 v101, 0x42000000, v105
	v_cvt_pk_fp8_f32 v99, v100, v101 op_sel:[0,0,1]
	v_lshl_add_u32 v102, s64, 6, v195
	v_mov_b64_e32 v[100:101], s[54:55]
	v_mad_i64_i32 v[100:101], s[54:55], s56, v102, v[100:101]
	v_lshl_add_u64 v[100:101], v[100:101], 0, s[30:31]
	v_lshl_add_u64 v[100:101], v[100:101], 0, v[192:193]
	s_cmpk_lt_i32 s21, 0x180
	global_store_dwordx2 v[100:101], v[98:99], off
	s_mov_b32 s100, 1
	s_cbranch_scc1 .LBB0_834
	v_sub_u32_e64 v98, s21, v251 clamp
	s_mov_b64 s[58:59], 0
	v_readfirstlane_b32 s2, v98
	s_addk_i32 s2, 0x17f
	s_mul_hi_u32 s2, s2, 0xaaaaaaab
	s_lshr_b32 s2, s2, 8
	s_mul_i32 s3, s2, 0xfffffe80
	s_add_i32 s3, s21, s3
	s_add_i32 s2, s33, s2
	s_add_i32 s21, s3, 0xfffffe80
	s_add_i32 s57, s2, 1

; __global__ void __launch_bounds__(NTHREADS, 2) fwd(const Params p) {
	.amdhsa_kernel _Z3fwd6Params
		.amdhsa_group_segment_fixed_size 0
		.amdhsa_private_segment_fixed_size 0
		.amdhsa_kernarg_size 496
		.amdhsa_user_sgpr_count 2
		.amdhsa_user_sgpr_dispatch_ptr 0
		.amdhsa_user_sgpr_queue_ptr 0
		.amdhsa_user_sgpr_kernarg_segment_ptr 1
		.amdhsa_user_sgpr_dispatch_id 0
		.amdhsa_user_sgpr_kernarg_preload_length 0
		.amdhsa_user_sgpr_kernarg_preload_offset 0
		.amdhsa_user_sgpr_private_segment_size 0
		.amdhsa_uses_dynamic_stack 0
		.amdhsa_enable_private_segment 0
		.amdhsa_system_sgpr_workgroup_id_x 1
		.amdhsa_system_sgpr_workgroup_id_y 0
		.amdhsa_system_sgpr_workgroup_id_z 0
		.amdhsa_system_sgpr_workgroup_info 0
		.amdhsa_system_vgpr_workitem_id 0
		.amdhsa_next_free_vgpr 256
		.amdhsa_next_free_sgpr 102
		.amdhsa_accum_offset 256
		.amdhsa_reserve_vcc 1
		.amdhsa_float_round_mode_32 0
		.amdhsa_float_round_mode_16_64 0
		.amdhsa_float_denorm_mode_32 3
		.amdhsa_float_denorm_mode_16_64 3
		.amdhsa_dx10_clamp 1
		.amdhsa_ieee_mode 1
		.amdhsa_fp16_overflow 0
		.amdhsa_tg_split 0
		.amdhsa_exception_fp_ieee_invalid_op 0
		.amdhsa_exception_fp_denorm_src 0
		.amdhsa_exception_fp_ieee_div_zero 0
		.amdhsa_exception_fp_ieee_overflow 0
		.amdhsa_exception_fp_ieee_underflow 0
		.amdhsa_exception_fp_ieee_inexact 0
		.amdhsa_exception_int_div_zero 0
	.end_amdhsa_kernel

; __global__ void __launch_bounds__(NTHREADS, 2) fwd(const Params p) {
amdhsa.kernels:
  - .agpr_count:     0
    .args:
      - .offset:         0
        .size:           240
        .value_kind:     by_value
      - .offset:         240
        .size:           4
        .value_kind:     hidden_block_count_x
      - .offset:         244
        .size:           4
        .value_kind:     hidden_block_count_y
      - .offset:         248
        .size:           4
        .value_kind:     hidden_block_count_z
      - .offset:         252
        .size:           2
        .value_kind:     hidden_group_size_x
      - .offset:         254
        .size:           2
        .value_kind:     hidden_group_size_y
      - .offset:         256
        .size:           2
        .value_kind:     hidden_group_size_z
      - .offset:         258
        .size:           2
        .value_kind:     hidden_remainder_x
      - .offset:         260
        .size:           2
        .value_kind:     hidden_remainder_y
      - .offset:         262
        .size:           2
        .value_kind:     hidden_remainder_z
      - .offset:         280
        .size:           8
        .value_kind:     hidden_global_offset_x
      - .offset:         288
        .size:           8
        .value_kind:     hidden_global_offset_y
      - .offset:         296
        .size:           8
        .value_kind:     hidden_global_offset_z
      - .offset:         304
        .size:           2
        .value_kind:     hidden_grid_dims
      - .offset:         360
        .size:           4
        .value_kind:     hidden_dynamic_lds_size
    .group_segment_fixed_size: 0
    .kernarg_segment_align: 8
    .kernarg_segment_size: 496
    .language:       OpenCL C
    .language_version:
      - 2
      - 0
    .max_flat_workgroup_size: 512
    .name:           _Z3fwd6Params
    .private_segment_fixed_size: 0
    .sgpr_count:     108
    .sgpr_spill_count: 218
    .symbol:         _Z3fwd6Params.kd
    .uniform_work_group_size: 1
    .uses_dynamic_stack: false
    .vgpr_count:     256
    .vgpr_spill_count: 0
    .wavefront_size: 64
